# L1/L2: W tile relocated in LDS with 544-B row stride so ds_read_b128 fragment reads are bank-conflict-free
# speedup vs baseline: 1.0087x; 1.0036x over previous
_Z7k_layerILi1EEvPKDF16_PKiPKjS3_S3_S1_PKfPDF16_PhS3_S7_Pf:
	s_load_dwordx2 s[24:25], s[0:1], 0x50
	s_load_dwordx8 s[8:15], s[0:1], 0x0
	s_load_dwordx8 s[16:23], s[0:1], 0x20
	v_lshrrev_b32_e32 v2, 5, v0
	v_and_b32_e32 v4, 31, v0
	v_mul_u32_u24_e32 v3, 0x220, v2
	v_lshlrev_b32_e32 v5, 4, v4
	v_or_b32_e32 v1, 0xfffffc00, v0
	v_add3_u32 v4, v3, v5, 0
	v_add_u32_e32 v4, 0x1cd90, v4
	v_lshl_or_b32 v2, v2, 9, v5
	v_mov_b32_e32 v3, 0
	s_waitcnt lgkmcnt(0)
	v_add_u32_e32 v3, 0x4000, v2
	v_lshlrev_b32_e32 v30, 4, v0
	v_cmp_gt_u32_e64 s[34:35], 16, v0
	v_lshrrev_b32_e32 v39, 6, v0
	s_and_saveexec_b64 s[4:5], s[34:35]
	global_load_dwordx4 v[42:45], v30, s[20:21]
	s_mov_b64 exec, s[4:5]
	global_load_dwordx4 v[6:9], v2, s[18:19]
	global_load_dwordx4 v[10:13], v3, s[18:19]
	v_add_u32_e32 v31, 0x4000, v30
	v_add_u32_e32 v32, 0x8000, v30
	v_add_u32_e32 v33, 0xc000, v30
	global_load_dwordx4 v[14:17], v30, s[8:9]
	global_load_dwordx4 v[18:21], v31, s[8:9]
	global_load_dwordx4 v[22:25], v32, s[8:9]
	global_load_dwordx4 v[26:29], v33, s[8:9]
	v_readfirstlane_b32 s36, v39
	v_mov_b32_e32 v40, v4
	v_add_u32_e32 v41, 0xcc10, v30
	v_add_u32_e32 v38, 0x1cc90, v30
	v_cmp_gt_u32_e32 vcc, 64, v0
	s_and_saveexec_b64 s[4:5], vcc
	v_lshl_add_u32 v1, v0, 1, 0
	v_add_u32_e32 v1, 0x1cc10, v1
	v_mov_b32_e32 v2, 0
	ds_write_b16 v1, v2
	s_mov_b64 exec, s[4:5]
	v_cmp_eq_u32_e32 vcc, 0, v0
	s_and_saveexec_b64 s[4:5], vcc
	v_mov_b32_e32 v1, 0
	v_mov_b32_e32 v2, 16
	ds_write_b32 v1, v2 offset:52224
	s_mov_b64 exec, s[4:5]
	s_mul_i32 s8, s2, 0x186a0
	s_lshr_b32 s8, s8, 8
	s_add_i32 s3, s2, 1
	s_mul_i32 s18, s3, 0x186a0
	s_lshr_b32 s18, s18, 8
.LBB4_14:
	v_lshrrev_b32_e32 v2, 3, v0
	s_load_dwordx2 s[4:5], s[0:1], 0x40
	v_and_b32_e32 v2, 0x78, v2
	s_movk_i32 s2, 0x90
	v_and_b32_e32 v97, 7, v0
	s_sub_i32 s0, s18, s8
	v_and_b32_e32 v1, 63, v0
	v_mov_b32_e32 v89, 0
	v_mad_u32_u24 v3, v2, s2, 0
	v_bfe_u32 v96, v0, 3, 3
	v_and_b32_e32 v99, 15, v0
	v_bfe_u32 v4, v0, 4, 2
	s_add_i32 s0, s0, 7
	v_mul_u32_u24_e32 v5, 0x90, v97
	v_and_b32_e32 v0, 48, v0
	s_ashr_i32 s9, s0, 3
	v_cmp_eq_u32_e64 s[0:1], 0, v1
	v_mad_u32_u24 v1, v96, s2, v3
	v_lshlrev_b32_e32 v2, 3, v4
	v_add3_u32 v103, v3, v5, v0
	v_mov_b32_e32 v3, v89
	v_lshlrev_b32_e32 v98, 4, v97
	v_add_u32_e32 v0, 0, v0
	v_lshlrev_b32_e32 v88, 2, v4
	v_lshl_add_u64 v[90:91], s[22:23], 0, v[2:3]
	v_mul_u32_u24_e32 v2, 0x220, v99
	v_or_b32_e32 v100, 8, v97
	v_or_b32_e32 v101, 16, v97
	v_add_u32_e32 v102, 0, v98
	v_cmp_gt_u32_e64 s[2:3], 8, v99
	s_waitcnt lgkmcnt(0)
	v_lshl_add_u64 v[92:93], s[4:5], 0, v[88:89]
	v_lshlrev_b32_e32 v88, 2, v88
	v_add_u32_e32 v104, v1, v98
	v_add_u32_e32 v105, v0, v2
	v_add_u32_e32 v105, 0x1cd90, v105
	s_lshl_b32 s19, s36, 3
	s_add_i32 s19, s19, s8
	v_add_u32_e32 v94, s19, v96
	v_cmp_gt_i32_e64 s[4:5], s18, v94
	v_mov_b32_e32 v32, 0
	v_mov_b32_e32 v33, 0
	v_mov_b32_e32 v34, 0
	v_mov_b32_e32 v35, 0
	s_and_saveexec_b64 s[6:7], s[4:5]
	v_lshl_add_u32 v36, v94, 1, v94
	v_lshlrev_b32_e32 v36, 2, v36
	global_load_dwordx4 v[32:35], v36, s[10:11]
	s_mov_b64 exec, s[6:7]
	s_waitcnt vmcnt(6)
	ds_write_b128 v40, v[6:9]
	s_waitcnt vmcnt(5)
	ds_write_b128 v40, v[10:13] offset:17408
	s_waitcnt vmcnt(4)
	ds_write_b128 v41, v[14:17]
	s_waitcnt vmcnt(3)
	ds_write_b128 v41, v[18:21] offset:16384
	s_waitcnt vmcnt(2)
	ds_write_b128 v41, v[22:25] offset:32768
	s_waitcnt vmcnt(1)
	ds_write_b128 v41, v[26:29] offset:49152
	s_and_saveexec_b64 s[6:7], s[34:35]
	ds_write_b128 v38, v[42:45]
	s_mov_b64 exec, s[6:7]
	s_waitcnt vmcnt(0)
	v_sub_u32_e32 v72, v33, v32
	v_sub_u32_e32 v108, v34, v33
	v_sub_u32_e32 v35, v35, v34
	v_add_lshl_u32 v37, v32, v97, 2
	v_add_lshl_u32 v38, v33, v97, 2
	v_add_lshl_u32 v39, v34, v97, 2
	v_mov_b32_e32 v36, 0x4000000
	v_mov_b32_e32 v68, 0x4000000
	v_mov_b32_e32 v74, 0x4000000
	v_mov_b32_e32 v85, 0x4000000
	v_mov_b32_e32 v84, 0x4000000
	v_mov_b32_e32 v109, 0x4000000
	v_mov_b32_e32 v107, 0x4000000
	v_mov_b32_e32 v106, 0x4000000
	v_mov_b32_e32 v95, 0x4000000
	s_mov_b64 s[6:7], exec
	v_cmp_lt_i32_e32 vcc, v97, v72
	s_and_b64 exec, exec, vcc
	global_load_dword v36, v37, s[12:13]
	v_cmp_lt_i32_e32 vcc, v100, v72
	s_and_b64 exec, exec, vcc
	global_load_dword v68, v37, s[12:13] offset:32
	v_cmp_lt_i32_e32 vcc, v101, v72
	s_and_b64 exec, exec, vcc
	global_load_dword v74, v37, s[12:13] offset:64
	s_mov_b64 exec, s[6:7]
	v_cmp_lt_i32_e32 vcc, v97, v108
	s_and_b64 exec, exec, vcc
	global_load_dword v85, v38, s[12:13]
	v_cmp_lt_i32_e32 vcc, v100, v108
	s_and_b64 exec, exec, vcc
	global_load_dword v84, v38, s[12:13] offset:32
	v_cmp_lt_i32_e32 vcc, v101, v108
	s_and_b64 exec, exec, vcc
	global_load_dword v109, v38, s[12:13] offset:64
	s_mov_b64 exec, s[6:7]
	v_cmp_lt_i32_e32 vcc, v97, v35
	s_and_b64 exec, exec, vcc
	global_load_dword v107, v39, s[12:13]
	v_cmp_lt_i32_e32 vcc, v100, v35
	s_and_b64 exec, exec, vcc
	global_load_dword v106, v39, s[12:13] offset:32
	v_cmp_lt_i32_e32 vcc, v101, v35
	s_and_b64 exec, exec, vcc
	global_load_dword v95, v39, s[12:13] offset:64
	s_mov_b64 exec, s[6:7]
	s_waitcnt lgkmcnt(0)
	s_barrier
	s_cmp_ge_i32 s36, s9
	s_cbranch_scc1 .LBB4_103
	s_branch .Lp1_after_idx

.LBB4_61:
	ds_write_b128 v104, v[52:55] offset:33792
	ds_read_b128 v[36:39], v105
	ds_read_b128 v[40:43], v103 offset:33792
	ds_read_b128 v[44:47], v105 offset:8704
	ds_read_b128 v[48:51], v105 offset:17408
	ds_read_b128 v[52:55], v105 offset:26112
	s_waitcnt lgkmcnt(3)
	v_mfma_f32_16x16x32_f16 v[36:39], v[36:39], v[40:43], 0
	s_waitcnt lgkmcnt(2)
	v_mfma_f32_16x16x32_f16 v[44:47], v[44:47], v[40:43], 0
	s_waitcnt lgkmcnt(1)
	v_mfma_f32_16x16x32_f16 v[48:51], v[48:51], v[40:43], 0
	s_waitcnt lgkmcnt(0)
	v_mfma_f32_16x16x32_f16 v[52:55], v[52:55], v[40:43], 0
	ds_read_b128 v[40:43], v105 offset:64
	ds_read_b128 v[56:59], v103 offset:33856
	ds_read_b128 v[60:63], v105 offset:8768
	ds_read_b128 v[64:67], v105 offset:17472
	s_waitcnt lgkmcnt(2)
	v_mfma_f32_16x16x32_f16 v[36:39], v[40:43], v[56:59], v[36:39]
	v_cmp_lt_i32_e32 vcc, 8, v108
	s_cmp_lg_u64 vcc, 0
	v_add_u32_dpp v32, v85, v102 row_newbcast:0 row_mask:0xf bank_mask:0x3
	v_add_u32_dpp v32, v85, v102 row_newbcast:8 row_mask:0xf bank_mask:0xc
	s_waitcnt lgkmcnt(1)
	v_mfma_f32_16x16x32_f16 v[40:43], v[60:63], v[56:59], v[44:47]
	ds_read_b128 v[60:63], v105 offset:26176
	ds_read_b128 v[68:71], v32 offset:52240
	s_waitcnt lgkmcnt(2)
	v_mfma_f32_16x16x32_f16 v[44:47], v[64:67], v[56:59], v[48:51]
	v_add_u32_dpp v64, v85, v102 row_newbcast:1 row_mask:0xf bank_mask:0x3
	v_add_u32_dpp v64, v85, v102 row_newbcast:9 row_mask:0xf bank_mask:0xc
	s_cselect_b64 s[22:23], -1, 0
	v_cmp_lt_i32_e64 s[6:7], 12, v108
	s_waitcnt lgkmcnt(1)
	v_mfma_f32_16x16x32_f16 v[48:51], v[60:63], v[56:59], v[52:55]
	v_add_u32_dpp v32, v85, v102 row_newbcast:2 row_mask:0xf bank_mask:0x3
	v_add_u32_dpp v32, v85, v102 row_newbcast:10 row_mask:0xf bank_mask:0xc
	s_nop 0
	ds_read_b128 v[76:79], v64 offset:52240
	ds_read_b128 v[72:75], v32 offset:52240
	v_add_u32_dpp v32, v85, v102 row_newbcast:3 row_mask:0xf bank_mask:0x3
	v_add_u32_dpp v32, v85, v102 row_newbcast:11 row_mask:0xf bank_mask:0xc
	v_add_u32_dpp v52, v85, v102 row_newbcast:4 row_mask:0xf bank_mask:0x3
	v_add_u32_dpp v52, v85, v102 row_newbcast:12 row_mask:0xf bank_mask:0xc
	ds_read_b128 v[80:83], v32 offset:52240
	ds_read_b128 v[52:55], v52 offset:52240
	v_add_u32_dpp v56, v85, v102 row_newbcast:5 row_mask:0xf bank_mask:0x3
	v_add_u32_dpp v56, v85, v102 row_newbcast:13 row_mask:0xf bank_mask:0xc
	v_add_u32_dpp v57, v85, v102 row_newbcast:6 row_mask:0xf bank_mask:0x3
	v_add_u32_dpp v57, v85, v102 row_newbcast:14 row_mask:0xf bank_mask:0xc
	ds_read_b128 v[60:63], v56 offset:52240
	ds_read_b128 v[64:67], v57 offset:52240
	v_add_u32_dpp v32, v85, v102 row_newbcast:7 row_mask:0xf bank_mask:0x3
	v_add_u32_dpp v32, v85, v102 row_newbcast:15 row_mask:0xf bank_mask:0xc
	ds_read_b128 v[56:59], v32 offset:52240
	s_cbranch_vccz .LBB4_63
	v_add_u32_dpp v0, v84, v102 row_newbcast:0 row_mask:0xf bank_mask:0x3
	v_add_u32_dpp v0, v84, v102 row_newbcast:8 row_mask:0xf bank_mask:0xc
	v_add_u32_dpp v8, v84, v102 row_newbcast:1 row_mask:0xf bank_mask:0x3
	v_add_u32_dpp v8, v84, v102 row_newbcast:9 row_mask:0xf bank_mask:0xc
	v_add_u32_dpp v16, v84, v102 row_newbcast:2 row_mask:0xf bank_mask:0x3
	v_add_u32_dpp v16, v84, v102 row_newbcast:10 row_mask:0xf bank_mask:0xc
	v_add_u32_dpp v24, v84, v102 row_newbcast:3 row_mask:0xf bank_mask:0x3
	v_add_u32_dpp v24, v84, v102 row_newbcast:11 row_mask:0xf bank_mask:0xc
	ds_read_b128 v[0:3], v0 offset:52240
	ds_read_b128 v[8:11], v8 offset:52240
	ds_read_b128 v[16:19], v16 offset:52240
	ds_read_b128 v[24:27], v24 offset:52240

.LBB4_80:
	ds_write_b128 v104, v[68:71] offset:33792
	ds_read_b128 v[52:55], v105 offset:128
	ds_read_b128 v[56:59], v103 offset:33792
	ds_read_b128 v[60:63], v105 offset:8832
	s_waitcnt lgkmcnt(1)
	v_mfma_f32_16x16x32_f16 v[36:39], v[52:55], v[56:59], v[36:39]
	ds_read_b128 v[52:55], v105 offset:17536
	s_waitcnt lgkmcnt(1)
	v_mfma_f32_16x16x32_f16 v[40:43], v[60:63], v[56:59], v[40:43]
	s_waitcnt lgkmcnt(0)
	v_mfma_f32_16x16x32_f16 v[44:47], v[52:55], v[56:59], v[44:47]
	ds_read_b128 v[52:55], v105 offset:26240
	s_waitcnt lgkmcnt(0)
	v_mfma_f32_16x16x32_f16 v[48:51], v[52:55], v[56:59], v[48:51]
	ds_read_b128 v[52:55], v105 offset:192
	ds_read_b128 v[56:59], v103 offset:33856
	ds_read_b128 v[60:63], v105 offset:8896
	v_cmp_lt_i32_e32 vcc, 8, v35
	s_waitcnt lgkmcnt(1)
	v_mfma_f32_16x16x32_f16 v[36:39], v[52:55], v[56:59], v[36:39]
	ds_read_b128 v[52:55], v105 offset:17600
	v_add_u32_dpp v32, v107, v102 row_newbcast:0 row_mask:0xf bank_mask:0x3
	v_add_u32_dpp v32, v107, v102 row_newbcast:8 row_mask:0xf bank_mask:0xc
	ds_read_b128 v[68:71], v32 offset:52240
	s_waitcnt lgkmcnt(2)
	v_mfma_f32_16x16x32_f16 v[40:43], v[60:63], v[56:59], v[40:43]
	ds_read_b128 v[60:63], v105 offset:26304
	v_add_u32_dpp v33, v107, v102 row_newbcast:1 row_mask:0xf bank_mask:0x3
	v_add_u32_dpp v33, v107, v102 row_newbcast:9 row_mask:0xf bank_mask:0xc
	s_cmp_lg_u64 vcc, 0
	s_waitcnt lgkmcnt(2)
	v_mfma_f32_16x16x32_f16 v[44:47], v[52:55], v[56:59], v[44:47]
	v_add_u32_dpp v32, v107, v102 row_newbcast:2 row_mask:0xf bank_mask:0x3
	v_add_u32_dpp v32, v107, v102 row_newbcast:10 row_mask:0xf bank_mask:0xc
	ds_read_b128 v[76:79], v33 offset:52240
	ds_read_b128 v[72:75], v32 offset:52240
	s_waitcnt lgkmcnt(2)
	v_mfma_f32_16x16x32_f16 v[48:51], v[60:63], v[56:59], v[48:51]
	v_add_u32_dpp v32, v107, v102 row_newbcast:3 row_mask:0xf bank_mask:0x3
	v_add_u32_dpp v32, v107, v102 row_newbcast:11 row_mask:0xf bank_mask:0xc
	v_add_u32_dpp v33, v107, v102 row_newbcast:4 row_mask:0xf bank_mask:0x3
	v_add_u32_dpp v33, v107, v102 row_newbcast:12 row_mask:0xf bank_mask:0xc
	ds_read_b128 v[80:83], v32 offset:52240
	ds_read_b128 v[52:55], v33 offset:52240
	s_cselect_b64 s[22:23], -1, 0
	v_add_u32_dpp v33, v107, v102 row_newbcast:5 row_mask:0xf bank_mask:0x3
	v_add_u32_dpp v33, v107, v102 row_newbcast:13 row_mask:0xf bank_mask:0xc
	v_add_u32_dpp v56, v107, v102 row_newbcast:6 row_mask:0xf bank_mask:0x3
	v_add_u32_dpp v56, v107, v102 row_newbcast:14 row_mask:0xf bank_mask:0xc
	ds_read_b128 v[60:63], v33 offset:52240
	ds_read_b128 v[64:67], v56 offset:52240
	v_add_u32_dpp v32, v107, v102 row_newbcast:7 row_mask:0xf bank_mask:0x3
	v_add_u32_dpp v32, v107, v102 row_newbcast:15 row_mask:0xf bank_mask:0xc
	ds_read_b128 v[56:59], v32 offset:52240
	v_cmp_lt_i32_e64 s[6:7], 12, v35
	s_cbranch_vccz .LBB4_82
	v_add_u32_dpp v0, v106, v102 row_newbcast:0 row_mask:0xf bank_mask:0x3
	v_add_u32_dpp v0, v106, v102 row_newbcast:8 row_mask:0xf bank_mask:0xc
	v_add_u32_dpp v8, v106, v102 row_newbcast:1 row_mask:0xf bank_mask:0x3
	v_add_u32_dpp v8, v106, v102 row_newbcast:9 row_mask:0xf bank_mask:0xc
	v_add_u32_dpp v16, v106, v102 row_newbcast:2 row_mask:0xf bank_mask:0x3
	v_add_u32_dpp v16, v106, v102 row_newbcast:10 row_mask:0xf bank_mask:0xc
	v_add_u32_dpp v24, v106, v102 row_newbcast:3 row_mask:0xf bank_mask:0x3
	v_add_u32_dpp v24, v106, v102 row_newbcast:11 row_mask:0xf bank_mask:0xc
	ds_read_b128 v[0:3], v0 offset:52240
	ds_read_b128 v[8:11], v8 offset:52240
	ds_read_b128 v[16:19], v16 offset:52240
	ds_read_b128 v[24:27], v24 offset:52240

.LBB4_99:
	ds_write_b128 v104, v[68:71] offset:33792
	ds_read_b128 v[32:35], v105 offset:256
	ds_read_b128 v[52:55], v103 offset:33792
	ds_read_b128 v[56:59], v105 offset:8960
	s_waitcnt lgkmcnt(1)
	v_mfma_f32_16x16x32_f16 v[32:35], v[32:35], v[52:55], v[36:39]
	s_nop 2
	ds_read_b128 v[36:39], v105 offset:17664
	s_waitcnt lgkmcnt(1)
	v_mfma_f32_16x16x32_f16 v[40:43], v[56:59], v[52:55], v[40:43]
	s_waitcnt lgkmcnt(0)
	v_mfma_f32_16x16x32_f16 v[44:47], v[36:39], v[52:55], v[44:47]
	ds_read_b128 v[36:39], v105 offset:26368
	s_waitcnt lgkmcnt(0)
	v_mfma_f32_16x16x32_f16 v[52:55], v[36:39], v[52:55], v[48:51]
	ds_read_b128 v[36:39], v105 offset:320
	ds_read_b128 v[56:59], v103 offset:33856
	s_nop 0
	ds_read_b128 v[48:51], v105 offset:9024
	ds_read_b128 v[60:63], v105 offset:17728
	ds_read_b128 v[64:67], v105 offset:26432
	s_waitcnt lgkmcnt(3)
	v_mfma_f32_16x16x32_f16 v[32:35], v[36:39], v[56:59], v[32:35]
	s_waitcnt lgkmcnt(2)
	v_mfma_f32_16x16x32_f16 v[36:39], v[48:51], v[56:59], v[40:43]
	v_mov_b32_e32 v48, 0
	v_mov_b32_e32 v49, v48
	v_mov_b32_e32 v50, v48
	s_waitcnt lgkmcnt(1)
	v_mfma_f32_16x16x32_f16 v[40:43], v[60:63], v[56:59], v[44:47]
	v_mov_b32_e32 v51, v48
	s_waitcnt lgkmcnt(0)
	v_mfma_f32_16x16x32_f16 v[44:47], v[64:67], v[56:59], v[52:55]
	s_and_saveexec_b64 s[6:7], s[4:5]
	s_cbranch_execz .LBB4_101
	v_lshlrev_b32_e32 v48, 7, v114
	v_lshl_add_u32 v49, v115, 11, 0
	v_add3_u32 v48, v49, v48, v98
	ds_read_b128 v[48:51], v48 offset:52240
.LBB4_101:
	s_or_b64 exec, exec, s[6:7]
	s_waitcnt lgkmcnt(0)
	ds_write_b128 v104, v[48:51] offset:33792
	ds_read_b128 v[48:51], v105 offset:384
	ds_read_b128 v[52:55], v103 offset:33792
	ds_read_b128 v[56:59], v105 offset:9088
	s_waitcnt lgkmcnt(1)
	v_mfma_f32_16x16x32_f16 v[32:35], v[48:51], v[52:55], v[32:35]
	ds_read_b128 v[48:51], v105 offset:17792
	s_waitcnt lgkmcnt(1)
	v_mfma_f32_16x16x32_f16 v[36:39], v[56:59], v[52:55], v[36:39]
	s_waitcnt lgkmcnt(0)
	v_mfma_f32_16x16x32_f16 v[56:59], v[48:51], v[52:55], v[40:43]
	s_nop 2
	ds_read_b128 v[40:43], v105 offset:26496
	s_waitcnt lgkmcnt(0)
	v_mfma_f32_16x16x32_f16 v[50:53], v[40:43], v[52:55], v[44:47]
	ds_read_b128 v[40:43], v105 offset:448
	ds_read_b128 v[60:63], v103 offset:33856
	ds_read_b128 v[64:67], v105 offset:9152
	v_add_u32_e32 v48, s19, v99
	v_cmp_gt_i32_e32 vcc, s18, v48
	s_and_b64 s[4:5], s[2:3], vcc
	s_waitcnt lgkmcnt(1)
	v_mfma_f32_16x16x32_f16 v[44:47], v[40:43], v[60:63], v[32:35]
	s_mov_b64 s[6:7], s[20:21]
	s_mov_b64 s[22:23], s[24:25]
	s_nop 0
	ds_read_b128 v[32:35], v105 offset:17856
	s_waitcnt lgkmcnt(1)
	v_mfma_f32_16x16x32_f16 v[40:43], v[64:67], v[60:63], v[36:39]
	ds_read_b128 v[64:67], v105 offset:26560
	s_waitcnt lgkmcnt(1)
	v_mfma_f32_16x16x32_f16 v[36:39], v[32:35], v[60:63], v[56:59]
	s_waitcnt lgkmcnt(0)
	v_mfma_f32_16x16x32_f16 v[32:35], v[64:67], v[60:63], v[50:53]
	s_and_saveexec_b64 s[22:23], s[4:5]
	s_xor_b64 s[4:5], exec, s[22:23]
	s_cbranch_execz .LBB4_15
	v_add_u32_e32 v50, 0x1cc90, v88
	ds_read_b128 v[52:55], v50
	v_mov_b32_e32 v56, v89
	s_waitcnt lgkmcnt(0)
	v_add_f32_e32 v44, v44, v52
	v_add_f32_e32 v45, v45, v53
	v_max_f32_e32 v57, 0, v44
	v_max_f32_e32 v58, 0, v45
	v_mul_f32_e32 v44, 0x42800000, v57
	v_mul_f32_e32 v45, 0x42800000, v58
	v_min_f32_e32 v44, 0x43e00000, v44
	v_min_f32_e32 v45, 0x43e00000, v45
	v_add_f32_e32 v46, v46, v54
	v_add_f32_e32 v47, v47, v55
	v_cvt_pk_fp8_f32 v56, v44, v45
	v_max_f32_e32 v46, 0, v46
	v_max_f32_e32 v47, 0, v47
	v_mul_f32_e32 v49, 0x42800000, v46
	v_mul_f32_e32 v44, 0x42800000, v47
	v_min_f32_e32 v45, 0x43e00000, v49
	v_min_f32_e32 v44, 0x43e00000, v44
	v_cvt_pk_fp8_f32 v56, v45, v44 op_sel:[0,0,1]
	v_ashrrev_i32_e32 v49, 31, v48
	v_lshlrev_b64 v[44:45], 6, v[48:49]
	v_lshl_add_u64 v[44:45], v[92:93], 0, v[44:45]
	global_store_dword v[44:45], v56, off
	ds_read_b128 v[52:55], v50 offset:64
	v_mov_b32_e32 v56, v89
	s_waitcnt lgkmcnt(0)
	v_add_f32_e32 v40, v40, v52
	v_add_f32_e32 v41, v41, v53
	v_max_f32_e32 v52, 0, v40
	v_max_f32_e32 v53, 0, v41
	v_mul_f32_e32 v40, 0x42800000, v52
	v_mul_f32_e32 v41, 0x42800000, v53
	v_min_f32_e32 v40, 0x43e00000, v40
	v_min_f32_e32 v41, 0x43e00000, v41
	v_add_f32_e32 v42, v42, v54
	v_add_f32_e32 v43, v43, v55
	v_cvt_pk_fp8_f32 v56, v40, v41
	v_max_f32_e32 v54, 0, v42
	v_max_f32_e32 v55, 0, v43
	v_mul_f32_e32 v42, 0x42800000, v54
	v_mul_f32_e32 v40, 0x42800000, v55
	v_min_f32_e32 v41, 0x43e00000, v42
	v_min_f32_e32 v40, 0x43e00000, v40
	v_cvt_pk_fp8_f32 v56, v41, v40 op_sel:[0,0,1]
	global_store_dword v[44:45], v56, off offset:16
	ds_read_b128 v[40:43], v50 offset:128
	v_mov_b32_e32 v56, v89
	s_waitcnt lgkmcnt(0)
	v_add_f32_e32 v36, v36, v40
	v_add_f32_e32 v37, v37, v41
	v_max_f32_e32 v59, 0, v36
	v_max_f32_e32 v60, 0, v37
	v_mul_f32_e32 v36, 0x42800000, v59
	v_mul_f32_e32 v37, 0x42800000, v60
	v_min_f32_e32 v36, 0x43e00000, v36
	v_min_f32_e32 v37, 0x43e00000, v37
	v_add_f32_e32 v38, v38, v42
	v_add_f32_e32 v39, v39, v43
	v_cvt_pk_fp8_f32 v56, v36, v37
	v_max_f32_e32 v61, 0, v38
	v_max_f32_e32 v62, 0, v39
	v_mul_f32_e32 v38, 0x42800000, v61
	v_mul_f32_e32 v36, 0x42800000, v62
	v_min_f32_e32 v37, 0x43e00000, v38
	v_min_f32_e32 v36, 0x43e00000, v36
	v_cvt_pk_fp8_f32 v56, v37, v36 op_sel:[0,0,1]
	v_lshlrev_b64 v[40:41], 7, v[48:49]
	v_lshl_add_u64 v[40:41], v[90:91], 0, v[40:41]
	v_cvt_pk_f16_f32 v43, v46, v47
	global_store_dword v[44:45], v56, off offset:32
	ds_read_b128 v[36:39], v50 offset:192
	v_cvt_pk_f16_f32 v42, v57, v58
	global_store_dwordx2 v[40:41], v[42:43], off
	v_cvt_pk_f16_f32 v43, v54, v55
	v_cvt_pk_f16_f32 v42, v52, v53
	global_store_dwordx2 v[40:41], v[42:43], off offset:32
	v_cvt_pk_f16_f32 v43, v61, v62
	v_cvt_pk_f16_f32 v42, v59, v60
	global_store_dwordx2 v[40:41], v[42:43], off offset:64
	s_waitcnt lgkmcnt(0)
	v_add_f32_e32 v32, v32, v36
	v_add_f32_e32 v33, v33, v37
	v_add_f32_e32 v34, v34, v38
	v_add_f32_e32 v35, v35, v39
	v_max_f32_e32 v32, 0, v32
	v_max_f32_e32 v36, 0, v33
	v_max_f32_e32 v33, 0, v34
	v_max_f32_e32 v34, 0, v35
	v_mul_f32_e32 v35, 0x42800000, v32
	v_mul_f32_e32 v37, 0x42800000, v36
	v_min_f32_e32 v35, 0x43e00000, v35
	v_min_f32_e32 v37, 0x43e00000, v37
	v_mov_b32_e32 v39, v89
	v_cvt_pk_fp8_f32 v39, v35, v37
	v_mul_f32_e32 v38, 0x42800000, v33
	v_mul_f32_e32 v37, 0x42800000, v34
	v_min_f32_e32 v35, 0x43e00000, v38
	v_min_f32_e32 v37, 0x43e00000, v37
	v_cvt_pk_fp8_f32 v39, v35, v37 op_sel:[0,0,1]
	v_cvt_pk_f16_f32 v33, v33, v34
	v_cvt_pk_f16_f32 v32, v32, v36
	global_store_dwordx2 v[40:41], v[32:33], off offset:96
	global_store_dword v[44:45], v39, off offset:48
	s_branch .LBB4_15

	.amdhsa_kernel _Z7k_layerILi1EEvPKDF16_PKiPKjS3_S3_S1_PKfPDF16_PhS3_S7_Pf
		.amdhsa_group_segment_fixed_size 35072
		.amdhsa_private_segment_fixed_size 0
		.amdhsa_kernarg_size 352
		.amdhsa_user_sgpr_count 2
		.amdhsa_user_sgpr_dispatch_ptr 0
		.amdhsa_user_sgpr_queue_ptr 0
		.amdhsa_user_sgpr_kernarg_segment_ptr 1
		.amdhsa_user_sgpr_dispatch_id 0
		.amdhsa_user_sgpr_kernarg_preload_length 0
		.amdhsa_user_sgpr_kernarg_preload_offset 0
		.amdhsa_user_sgpr_private_segment_size 0
		.amdhsa_uses_dynamic_stack 0
		.amdhsa_enable_private_segment 0
		.amdhsa_system_sgpr_workgroup_id_x 1
		.amdhsa_system_sgpr_workgroup_id_y 0
		.amdhsa_system_sgpr_workgroup_id_z 0
		.amdhsa_system_sgpr_workgroup_info 0
		.amdhsa_system_vgpr_workitem_id 0
		.amdhsa_next_free_vgpr 116
		.amdhsa_next_free_sgpr 37
		.amdhsa_accum_offset 116
		.amdhsa_reserve_vcc 1
		.amdhsa_float_round_mode_32 0
		.amdhsa_float_round_mode_16_64 0
		.amdhsa_float_denorm_mode_32 3
		.amdhsa_float_denorm_mode_16_64 3
		.amdhsa_dx10_clamp 1
		.amdhsa_ieee_mode 1
		.amdhsa_fp16_overflow 0
		.amdhsa_tg_split 0
		.amdhsa_exception_fp_ieee_invalid_op 0
		.amdhsa_exception_fp_denorm_src 0
		.amdhsa_exception_fp_ieee_div_zero 0
		.amdhsa_exception_fp_ieee_overflow 0
		.amdhsa_exception_fp_ieee_underflow 0
		.amdhsa_exception_fp_ieee_inexact 0
		.amdhsa_exception_int_div_zero 0
	.end_amdhsa_kernel

_Z7k_layerILi2EEvPKDF16_PKiPKjS3_S3_S1_PKfPDF16_PhS3_S7_Pf:
	s_load_dwordx2 s[24:25], s[0:1], 0x58
	s_load_dwordx4 s[12:15], s[0:1], 0x0
	s_load_dwordx2 s[26:27], s[0:1], 0x10
	s_load_dwordx4 s[16:19], s[0:1], 0x48
	s_load_dwordx4 s[20:23], s[0:1], 0x28
	v_lshrrev_b32_e32 v2, 5, v0
	v_and_b32_e32 v4, 31, v0
	v_mul_u32_u24_e32 v3, 0x220, v2
	v_lshlrev_b32_e32 v5, 4, v4
	v_add3_u32 v4, v3, v5, 0
	v_add_u32_e32 v4, 0xcf10, v4
	v_lshl_or_b32 v2, v2, 9, v5
	v_mov_b32_e32 v3, 0
	v_or_b32_e32 v1, 0xfffffc00, v0
	s_waitcnt lgkmcnt(0)
	v_add_u32_e32 v3, 0x4000, v2
	v_lshlrev_b32_e32 v14, 4, v0
	v_add_u32_e32 v15, 0xffffff00, v14
	v_lshrrev_b32_e32 v21, 6, v0
	s_mov_b64 s[4:5], exec
	v_cmp_gt_u32_e32 vcc, 16, v0
	v_cmp_gt_u32_e64 s[40:41], 48, v0
	s_andn2_b64 s[8:9], s[40:41], vcc
	s_and_b64 exec, s[4:5], vcc
	global_load_dwordx4 v[16:19], v14, s[22:23]
	s_and_b64 exec, s[4:5], s[8:9]
	global_load_dwordx4 v[16:19], v15, s[18:19]
	s_mov_b64 exec, s[4:5]
	global_load_dwordx4 v[22:25], v2, s[20:21]
	global_load_dwordx4 v[26:29], v3, s[20:21]
	v_readfirstlane_b32 s38, v21
	v_mov_b32_e32 v20, v4
	v_cmp_eq_u32_e32 vcc, 0, v0
	s_and_saveexec_b64 s[6:7], vcc
	v_mov_b32_e32 v1, 0
	v_mov_b32_e32 v2, 16
	ds_write_b32 v1, v2 offset:52224
	s_mov_b64 exec, s[6:7]
	s_mul_i32 s20, s2, 0x186a0
	s_lshr_b32 s20, s20, 8
	s_add_i32 s3, s2, 1
	s_mul_i32 s28, s3, 0x186a0
	s_lshr_b32 s28, s28, 8
.LBB5_10:
	v_lshrrev_b32_e32 v2, 3, v0
	s_load_dwordx2 s[30:31], s[0:1], 0x40
	v_and_b32_e32 v1, 63, v0
	v_and_b32_e32 v2, 0x78, v2
	s_movk_i32 s2, 0x90
	v_bfe_u32 v74, v0, 3, 3
	v_and_b32_e32 v75, 7, v0
	v_and_b32_e32 v77, 15, v0
	s_sub_i32 s0, s28, s20
	v_and_b32_e32 v5, 48, v0
	v_lshrrev_b32_e32 v0, 2, v0
	v_mad_u32_u24 v2, v2, s2, 0
	s_add_i32 s0, s0, 7
	v_mul_u32_u24_e32 v4, 0x90, v75
	v_and_b32_e32 v0, 12, v0
	v_lshlrev_b32_e32 v76, 4, v75
	s_ashr_i32 s21, s0, 3
	v_cmp_eq_u32_e64 s[0:1], 0, v1
	v_mad_u32_u24 v3, v74, s2, v2
	v_add3_u32 v80, v2, v4, v5
	v_add_u32_e32 v2, 0, v5
	v_cmp_gt_u32_e64 s[4:5], 16, v1
	v_mul_u32_u24_e32 v1, 0x220, v77
	v_lshlrev_b32_e32 v32, 2, v0
	v_mbcnt_lo_u32_b32 v0, -1, 0
	v_mov_b32_e32 v33, 0
	v_or_b32_e32 v78, 8, v75
	v_or_b32_e32 v79, 16, v75
	v_lshlrev_b32_e32 v81, 3, v75
	v_cmp_gt_u32_e64 s[2:3], 8, v77
	s_mov_b32 s29, 0x3c800000
	v_add_u32_e32 v82, v3, v76
	v_add_u32_e32 v83, v2, v1
	v_add_u32_e32 v83, 0xcf10, v83
	v_mbcnt_hi_u32_b32 v84, -1, v0
	s_lshl_b32 s33, s38, 3
	s_add_i32 s33, s33, s20
	v_add_u32_e32 v8, s33, v74
	v_cmp_gt_i32_e32 vcc, s28, v8
	v_mov_b32_e32 v0, 0
	v_mov_b32_e32 v1, 0
	v_mov_b32_e32 v2, 0
	v_mov_b32_e32 v3, 0
	v_mov_b32_e32 v4, 0
	v_mov_b32_e32 v5, 0
	v_mov_b32_e32 v6, 0
	v_mov_b32_e32 v7, 0
	s_and_saveexec_b64 s[6:7], vcc
	v_lshl_add_u32 v9, v8, 1, v8
	v_lshlrev_b32_e32 v9, 2, v9
	global_load_dwordx4 v[4:7], v9, s[14:15]
	v_lshl_or_b32 v9, v8, 7, v76
	global_load_dwordx4 v[0:3], v9, s[12:13]
	s_mov_b64 exec, s[6:7]
	s_waitcnt vmcnt(3)
	ds_write_b128 v20, v[22:25]
	s_waitcnt vmcnt(2)
	ds_write_b128 v20, v[26:29] offset:17408
	s_and_saveexec_b64 s[6:7], s[40:41]
	ds_write_b128 v14, v[16:19] offset:52240
	s_mov_b64 exec, s[6:7]
	s_waitcnt vmcnt(1)
	v_sub_u32_e32 v58, v5, v4
	v_sub_u32_e32 v87, v6, v5
	v_sub_u32_e32 v85, v7, v6
	v_add_lshl_u32 v10, v4, v75, 2
	v_add_lshl_u32 v11, v5, v75, 2
	v_add_lshl_u32 v12, v6, v75, 2
	v_mov_b32_e32 v9, 0x186a0
	v_mov_b32_e32 v8, 0x186a0
	v_mov_b32_e32 v60, 0x186a0
	v_mov_b32_e32 v59, 0x186a0
	v_mov_b32_e32 v62, 0x186a0
	v_mov_b32_e32 v89, 0x186a0
	v_mov_b32_e32 v88, 0x186a0
	v_mov_b32_e32 v86, 0x186a0
	v_mov_b32_e32 v7, 0x186a0
	s_mov_b64 s[6:7], exec
	v_cmp_lt_i32_e32 vcc, v75, v58
	s_and_b64 exec, exec, vcc
	global_load_dword v9, v10, s[26:27]
	v_cmp_lt_i32_e32 vcc, v78, v58
	s_and_b64 exec, exec, vcc
	global_load_dword v8, v10, s[26:27] offset:32
	v_cmp_lt_i32_e32 vcc, v79, v58
	s_and_b64 exec, exec, vcc
	global_load_dword v60, v10, s[26:27] offset:64
	s_mov_b64 exec, s[6:7]
	v_cmp_lt_i32_e32 vcc, v75, v87
	s_and_b64 exec, exec, vcc
	global_load_dword v59, v11, s[26:27]
	v_cmp_lt_i32_e32 vcc, v78, v87
	s_and_b64 exec, exec, vcc
	global_load_dword v62, v11, s[26:27] offset:32
	v_cmp_lt_i32_e32 vcc, v79, v87
	s_and_b64 exec, exec, vcc
	global_load_dword v89, v11, s[26:27] offset:64
	s_mov_b64 exec, s[6:7]
	v_cmp_lt_i32_e32 vcc, v75, v85
	s_and_b64 exec, exec, vcc
	global_load_dword v88, v12, s[26:27]
	v_cmp_lt_i32_e32 vcc, v78, v85
	s_and_b64 exec, exec, vcc
	global_load_dword v86, v12, s[26:27] offset:32
	v_cmp_lt_i32_e32 vcc, v79, v85
	s_and_b64 exec, exec, vcc
	global_load_dword v7, v12, s[26:27] offset:64
	s_mov_b64 exec, s[6:7]
	s_waitcnt lgkmcnt(0)
	s_barrier
	s_cmp_ge_i32 s38, s21
	s_cbranch_scc1 .LBB5_118
	s_branch .Lp2_after_idx

.LBB5_61:
	s_cbranch_execz .LBB5_58
	ds_write_b128 v82, v[8:11] offset:33792
	ds_read_b128 v[8:11], v83
	ds_read_b128 v[12:15], v80 offset:33792
	ds_read_b128 v[16:19], v83 offset:8704
	ds_read_b128 v[20:23], v83 offset:17408
	ds_read_b128 v[24:27], v83 offset:26112
	s_waitcnt lgkmcnt(3)
	v_mfma_f32_16x16x32_f16 v[8:11], v[8:11], v[12:15], 0
	s_waitcnt lgkmcnt(2)
	v_mfma_f32_16x16x32_f16 v[16:19], v[16:19], v[12:15], 0
	s_waitcnt lgkmcnt(1)
	v_mfma_f32_16x16x32_f16 v[20:23], v[20:23], v[12:15], 0
	s_waitcnt lgkmcnt(0)
	v_mfma_f32_16x16x32_f16 v[90:93], v[24:27], v[12:15], 0
	ds_read_b128 v[12:15], v83 offset:64
	ds_read_b128 v[94:97], v80 offset:33856
	ds_read_b128 v[24:27], v83 offset:8768
	ds_read_b128 v[98:101], v83 offset:17472
	s_waitcnt lgkmcnt(2)
	v_mfma_f32_16x16x32_f16 v[8:11], v[12:15], v[94:97], v[8:11]
	v_add_u32_dpp v4, v59, v81 row_newbcast:0 row_mask:0xf bank_mask:0x3
	v_add_u32_dpp v4, v59, v81 row_newbcast:8 row_mask:0xf bank_mask:0xc
	s_waitcnt lgkmcnt(1)
	v_mfma_f32_16x16x32_f16 v[12:15], v[24:27], v[94:97], v[16:19]
	v_mov_b32_dpp v24, v59 row_newbcast:5 row_mask:0xf bank_mask:0x3
	v_mov_b32_dpp v24, v59 row_newbcast:13 row_mask:0xf bank_mask:0xc
	v_mov_b32_dpp v25, v59 row_newbcast:6 row_mask:0xf bank_mask:0x3
	v_mov_b32_dpp v25, v59 row_newbcast:14 row_mask:0xf bank_mask:0xc
	v_mov_b32_dpp v26, v59 row_newbcast:7 row_mask:0xf bank_mask:0x3
	v_mov_b32_dpp v26, v59 row_newbcast:15 row_mask:0xf bank_mask:0xc
	v_mov_b32_dpp v19, v59 row_newbcast:4 row_mask:0xf bank_mask:0x3
	v_mov_b32_dpp v19, v59 row_newbcast:12 row_mask:0xf bank_mask:0xc
	v_add_u32_dpp v16, v59, v81 row_newbcast:1 row_mask:0xf bank_mask:0x3
	v_add_u32_dpp v16, v59, v81 row_newbcast:9 row_mask:0xf bank_mask:0xc
	v_add_u32_dpp v17, v59, v81 row_newbcast:2 row_mask:0xf bank_mask:0x3
	v_add_u32_dpp v17, v59, v81 row_newbcast:10 row_mask:0xf bank_mask:0xc
	v_add_u32_dpp v18, v59, v81 row_newbcast:3 row_mask:0xf bank_mask:0x3
	v_add_u32_dpp v18, v59, v81 row_newbcast:11 row_mask:0xf bank_mask:0xc
	global_load_dwordx2 v[72:73], v4, s[30:31]
	global_load_dwordx2 v[68:69], v16, s[30:31]
	global_load_dwordx2 v[64:65], v17, s[30:31]
	global_load_dwordx2 v[58:59], v18, s[30:31]
	v_add_u32_e32 v4, v19, v81
	v_add_u32_e32 v16, v24, v81
	v_add_u32_e32 v17, v25, v81
	v_add_u32_e32 v18, v26, v81
	global_load_dwordx2 v[70:71], v4, s[30:31]
	global_load_dwordx2 v[66:67], v16, s[30:31]
	global_load_dwordx2 v[60:61], v17, s[30:31]
	global_load_dwordx2 v[54:55], v18, s[30:31]
	v_add_u32_dpp v4, v62, v81 row_newbcast:0 row_mask:0xf bank_mask:0x3
	v_add_u32_dpp v4, v62, v81 row_newbcast:8 row_mask:0xf bank_mask:0xc
	v_mov_b32_dpp v19, v62 row_newbcast:4 row_mask:0xf bank_mask:0x3
	v_mov_b32_dpp v19, v62 row_newbcast:12 row_mask:0xf bank_mask:0xc
	v_add_u32_dpp v16, v62, v81 row_newbcast:1 row_mask:0xf bank_mask:0x3
	v_add_u32_dpp v16, v62, v81 row_newbcast:9 row_mask:0xf bank_mask:0xc
	v_add_u32_dpp v17, v62, v81 row_newbcast:2 row_mask:0xf bank_mask:0x3
	v_add_u32_dpp v17, v62, v81 row_newbcast:10 row_mask:0xf bank_mask:0xc
	v_add_u32_dpp v18, v62, v81 row_newbcast:3 row_mask:0xf bank_mask:0x3
	v_add_u32_dpp v18, v62, v81 row_newbcast:11 row_mask:0xf bank_mask:0xc
	v_mov_b32_dpp v24, v62 row_newbcast:5 row_mask:0xf bank_mask:0x3
	v_mov_b32_dpp v24, v62 row_newbcast:13 row_mask:0xf bank_mask:0xc
	v_mov_b32_dpp v25, v62 row_newbcast:6 row_mask:0xf bank_mask:0x3
	v_mov_b32_dpp v25, v62 row_newbcast:14 row_mask:0xf bank_mask:0xc
	v_mov_b32_dpp v26, v62 row_newbcast:7 row_mask:0xf bank_mask:0x3
	v_mov_b32_dpp v26, v62 row_newbcast:15 row_mask:0xf bank_mask:0xc
	global_load_dwordx2 v[62:63], v4, s[30:31]
	global_load_dwordx2 v[56:57], v16, s[30:31]
	global_load_dwordx2 v[52:53], v17, s[30:31]
	global_load_dwordx2 v[50:51], v18, s[30:31]
	v_add_u32_e32 v4, v19, v81
	v_add_u32_e32 v16, v24, v81
	v_add_u32_e32 v17, v25, v81
	v_add_u32_e32 v18, v26, v81
	global_load_dwordx2 v[30:31], v4, s[30:31]
	global_load_dwordx2 v[28:29], v16, s[30:31]
	global_load_dwordx2 v[26:27], v17, s[30:31]
	global_load_dwordx2 v[24:25], v18, s[30:31]
	s_waitcnt lgkmcnt(0)
	v_mfma_f32_16x16x32_f16 v[16:19], v[98:101], v[94:97], v[20:23]
	v_cmp_lt_i32_e32 vcc, 16, v87
	s_cmp_lg_u64 vcc, 0
	s_cselect_b64 s[36:37], -1, 0
	ds_read_b128 v[20:23], v83 offset:26176
	s_waitcnt lgkmcnt(0)
	v_mfma_f32_16x16x32_f16 v[20:23], v[20:23], v[94:97], v[90:93]
	v_cmp_lt_i32_e64 s[10:11], 18, v87
	v_cmp_lt_i32_e64 s[8:9], 20, v87
	v_cmp_lt_i32_e64 s[6:7], 22, v87
	s_cbranch_vccz .LBB5_64
	v_add_u32_dpp v4, v89, v81 row_newbcast:0 row_mask:0xf bank_mask:0x3
	v_add_u32_dpp v4, v89, v81 row_newbcast:8 row_mask:0xf bank_mask:0xc
	v_add_u32_dpp v38, v89, v81 row_newbcast:1 row_mask:0xf bank_mask:0x3
	v_add_u32_dpp v38, v89, v81 row_newbcast:9 row_mask:0xf bank_mask:0xc
	global_load_dwordx2 v[34:35], v4, s[30:31]
	s_nop 0
	global_load_dwordx2 v[38:39], v38, s[30:31]

.LBB5_83:
	s_cbranch_execz .LBB5_80
	ds_write_b128 v82, v[24:27] offset:33792
	ds_read_b128 v[24:27], v83 offset:128
	ds_read_b128 v[28:31], v80 offset:33792
	ds_read_b128 v[50:53], v83 offset:8832
	s_waitcnt lgkmcnt(1)
	v_mfma_f32_16x16x32_f16 v[8:11], v[24:27], v[28:31], v[8:11]
	ds_read_b128 v[24:27], v83 offset:17536
	s_waitcnt lgkmcnt(1)
	v_mfma_f32_16x16x32_f16 v[12:15], v[50:53], v[28:31], v[12:15]
	s_waitcnt lgkmcnt(0)
	v_mfma_f32_16x16x32_f16 v[16:19], v[24:27], v[28:31], v[16:19]
	ds_read_b128 v[24:27], v83 offset:26240
	s_waitcnt lgkmcnt(0)
	v_mfma_f32_16x16x32_f16 v[20:23], v[24:27], v[28:31], v[20:23]
	ds_read_b128 v[24:27], v83 offset:192
	ds_read_b128 v[90:93], v80 offset:33856
	ds_read_b128 v[28:31], v83 offset:8896
	ds_read_b128 v[94:97], v83 offset:17600
	s_waitcnt lgkmcnt(2)
	v_mfma_f32_16x16x32_f16 v[8:11], v[24:27], v[90:93], v[8:11]
	s_waitcnt lgkmcnt(1)
	v_mfma_f32_16x16x32_f16 v[12:15], v[28:31], v[90:93], v[12:15]
	v_add_u32_dpp v4, v88, v81 row_newbcast:0 row_mask:0xf bank_mask:0x3
	v_add_u32_dpp v4, v88, v81 row_newbcast:8 row_mask:0xf bank_mask:0xc
	v_add_u32_dpp v5, v88, v81 row_newbcast:1 row_mask:0xf bank_mask:0x3
	v_add_u32_dpp v5, v88, v81 row_newbcast:9 row_mask:0xf bank_mask:0xc
	v_add_u32_dpp v24, v88, v81 row_newbcast:2 row_mask:0xf bank_mask:0x3
	v_add_u32_dpp v24, v88, v81 row_newbcast:10 row_mask:0xf bank_mask:0xc
	v_add_u32_dpp v25, v88, v81 row_newbcast:3 row_mask:0xf bank_mask:0x3
	v_add_u32_dpp v25, v88, v81 row_newbcast:11 row_mask:0xf bank_mask:0xc
	global_load_dwordx2 v[70:71], v4, s[30:31]
	global_load_dwordx2 v[66:67], v5, s[30:31]
	global_load_dwordx2 v[62:63], v24, s[30:31]
	global_load_dwordx2 v[56:57], v25, s[30:31]
	v_add_u32_dpp v4, v88, v81 row_newbcast:4 row_mask:0xf bank_mask:0x3
	v_add_u32_dpp v4, v88, v81 row_newbcast:12 row_mask:0xf bank_mask:0xc
	v_add_u32_dpp v5, v88, v81 row_newbcast:5 row_mask:0xf bank_mask:0x3
	v_add_u32_dpp v5, v88, v81 row_newbcast:13 row_mask:0xf bank_mask:0xc
	v_add_u32_dpp v24, v88, v81 row_newbcast:6 row_mask:0xf bank_mask:0x3
	v_add_u32_dpp v24, v88, v81 row_newbcast:14 row_mask:0xf bank_mask:0xc
	v_add_u32_dpp v25, v88, v81 row_newbcast:7 row_mask:0xf bank_mask:0x3
	v_add_u32_dpp v25, v88, v81 row_newbcast:15 row_mask:0xf bank_mask:0xc
	global_load_dwordx2 v[68:69], v4, s[30:31]
	global_load_dwordx2 v[64:65], v5, s[30:31]
	global_load_dwordx2 v[58:59], v24, s[30:31]
	global_load_dwordx2 v[52:53], v25, s[30:31]
	v_add_u32_dpp v4, v86, v81 row_newbcast:0 row_mask:0xf bank_mask:0x3
	v_add_u32_dpp v4, v86, v81 row_newbcast:8 row_mask:0xf bank_mask:0xc
	v_add_u32_dpp v5, v86, v81 row_newbcast:1 row_mask:0xf bank_mask:0x3
	v_add_u32_dpp v5, v86, v81 row_newbcast:9 row_mask:0xf bank_mask:0xc
	v_add_u32_dpp v24, v86, v81 row_newbcast:2 row_mask:0xf bank_mask:0x3
	v_add_u32_dpp v24, v86, v81 row_newbcast:10 row_mask:0xf bank_mask:0xc
	v_add_u32_dpp v25, v86, v81 row_newbcast:3 row_mask:0xf bank_mask:0x3
	v_add_u32_dpp v25, v86, v81 row_newbcast:11 row_mask:0xf bank_mask:0xc
	global_load_dwordx2 v[60:61], v4, s[30:31]
	global_load_dwordx2 v[54:55], v5, s[30:31]
	global_load_dwordx2 v[50:51], v24, s[30:31]
	global_load_dwordx2 v[30:31], v25, s[30:31]
	v_add_u32_dpp v4, v86, v81 row_newbcast:4 row_mask:0xf bank_mask:0x3
	v_add_u32_dpp v4, v86, v81 row_newbcast:12 row_mask:0xf bank_mask:0xc
	v_add_u32_dpp v5, v86, v81 row_newbcast:5 row_mask:0xf bank_mask:0x3
	v_add_u32_dpp v5, v86, v81 row_newbcast:13 row_mask:0xf bank_mask:0xc
	v_add_u32_dpp v24, v86, v81 row_newbcast:6 row_mask:0xf bank_mask:0x3
	v_add_u32_dpp v24, v86, v81 row_newbcast:14 row_mask:0xf bank_mask:0xc
	v_add_u32_dpp v72, v86, v81 row_newbcast:7 row_mask:0xf bank_mask:0x3
	v_add_u32_dpp v72, v86, v81 row_newbcast:15 row_mask:0xf bank_mask:0xc
	global_load_dwordx2 v[28:29], v4, s[30:31]
	global_load_dwordx2 v[26:27], v5, s[30:31]
	s_nop 0
	global_load_dwordx2 v[24:25], v24, s[30:31]
	s_nop 0
	global_load_dwordx2 v[4:5], v72, s[30:31]
	ds_read_b128 v[86:89], v83 offset:26304
	s_waitcnt lgkmcnt(1)
	v_mfma_f32_16x16x32_f16 v[16:19], v[94:97], v[90:93], v[16:19]
	v_cmp_lt_i32_e32 vcc, 16, v85
	s_cmp_lg_u64 vcc, 0
	s_cselect_b64 s[36:37], -1, 0
	s_waitcnt lgkmcnt(0)
	v_mfma_f32_16x16x32_f16 v[20:23], v[86:89], v[90:93], v[20:23]
	v_cmp_lt_i32_e64 s[10:11], 18, v85
	v_cmp_lt_i32_e64 s[8:9], 20, v85
	v_cmp_lt_i32_e64 s[6:7], 22, v85
	s_cbranch_vccz .LBB5_86
	v_add_u32_dpp v34, v7, v81 row_newbcast:0 row_mask:0xf bank_mask:0x3
	v_add_u32_dpp v34, v7, v81 row_newbcast:8 row_mask:0xf bank_mask:0xc
	v_add_u32_dpp v38, v7, v81 row_newbcast:1 row_mask:0xf bank_mask:0x3
	v_add_u32_dpp v38, v7, v81 row_newbcast:9 row_mask:0xf bank_mask:0xc
	global_load_dwordx2 v[34:35], v34, s[30:31]
	s_nop 0
	global_load_dwordx2 v[38:39], v38, s[30:31]

.LBB5_105:
	s_cbranch_execz .LBB5_102
	ds_write_b128 v82, v[4:7] offset:33792
	ds_read_b128 v[4:7], v83 offset:256
	ds_read_b128 v[24:27], v80 offset:33792
	ds_read_b128 v[28:31], v83 offset:8960
	s_waitcnt lgkmcnt(1)
	v_mfma_f32_16x16x32_f16 v[4:7], v[4:7], v[24:27], v[8:11]
	s_nop 2
	ds_read_b128 v[8:11], v83 offset:17664
	s_waitcnt lgkmcnt(1)
	v_mfma_f32_16x16x32_f16 v[12:15], v[28:31], v[24:27], v[12:15]
	s_waitcnt lgkmcnt(0)
	v_mfma_f32_16x16x32_f16 v[8:11], v[8:11], v[24:27], v[16:19]
	s_nop 2
	ds_read_b128 v[16:19], v83 offset:26368
	s_waitcnt lgkmcnt(0)
	v_mfma_f32_16x16x32_f16 v[16:19], v[16:19], v[24:27], v[20:23]
	s_nop 2
	ds_read_b128 v[20:23], v83 offset:320
	ds_read_b128 v[24:27], v80 offset:33856
	ds_read_b128 v[28:31], v83 offset:9024
	s_waitcnt lgkmcnt(1)
	v_mfma_f32_16x16x32_f16 v[4:7], v[20:23], v[24:27], v[4:7]
	ds_read_b128 v[20:23], v83 offset:17728
	s_waitcnt lgkmcnt(1)
	v_mfma_f32_16x16x32_f16 v[12:15], v[28:31], v[24:27], v[12:15]
	s_waitcnt lgkmcnt(0)
	v_mfma_f32_16x16x32_f16 v[8:11], v[20:23], v[24:27], v[8:11]
	ds_read_b128 v[20:23], v83 offset:26432
	ds_write_b128 v82, v[0:3] offset:33792
	s_waitcnt lgkmcnt(1)
	v_mfma_f32_16x16x32_f16 v[0:3], v[20:23], v[24:27], v[16:19]
	s_nop 2
	ds_read_b128 v[16:19], v83 offset:384
	ds_read_b128 v[20:23], v80 offset:33792
	ds_read_b128 v[24:27], v83 offset:9088
	s_waitcnt lgkmcnt(1)
	v_mfma_f32_16x16x32_f16 v[4:7], v[16:19], v[20:23], v[4:7]
	ds_read_b128 v[16:19], v83 offset:17792
	s_waitcnt lgkmcnt(1)
	v_mfma_f32_16x16x32_f16 v[12:15], v[24:27], v[20:23], v[12:15]
	s_waitcnt lgkmcnt(0)
	v_mfma_f32_16x16x32_f16 v[8:11], v[16:19], v[20:23], v[8:11]
	ds_read_b128 v[16:19], v83 offset:26496
	s_waitcnt lgkmcnt(0)
	v_mfma_f32_16x16x32_f16 v[0:3], v[16:19], v[20:23], v[0:3]
	ds_read_b128 v[16:19], v83 offset:448
	ds_read_b128 v[20:23], v80 offset:33856
	ds_read_b128 v[24:27], v83 offset:9152
	ds_read_b128 v[28:31], v83 offset:17856
	ds_read_b128 v[50:53], v83 offset:26560
	s_mov_b64 s[6:7], s[22:23]
	s_mov_b64 s[8:9], s[18:19]
	s_waitcnt lgkmcnt(1)
	v_mfma_f32_16x16x32_f16 v[8:11], v[28:31], v[20:23], v[8:11]
	s_nop 0
	s_waitcnt lgkmcnt(0)
	v_mfma_f32_16x16x32_f16 v[0:3], v[50:53], v[20:23], v[0:3]
	v_mfma_f32_16x16x32_f16 v[16:19], v[16:19], v[20:23], v[4:7]
	s_nop 2
	v_add_u32_e32 v6, s33, v77
	v_mfma_f32_16x16x32_f16 v[12:15], v[24:27], v[20:23], v[12:15]
	v_cmp_gt_i32_e32 vcc, s28, v6
	ds_read_b128 v[20:23], v32 offset:52240
	ds_read_b128 v[24:27], v32 offset:52496
	ds_read_b128 v[28:31], v32 offset:52752
	s_waitcnt lgkmcnt(2)
	v_add_f32_e32 v7, v16, v20
	s_waitcnt lgkmcnt(1)
	v_mov_b32_e32 v4, v24
	s_waitcnt lgkmcnt(0)
	v_mov_b32_e32 v5, v28
	v_add_f32_e32 v16, v17, v21
	v_add_f32_e32 v17, v18, v22
	v_add_f32_e32 v18, v19, v23
	v_max_f32_e32 v24, 0, v7
	v_max_f32_e32 v62, 0, v16
	v_max_f32_e32 v64, 0, v17
	v_max_f32_e32 v66, 0, v18
	ds_read_b128 v[16:19], v32 offset:52304
	ds_read_b128 v[20:23], v32 offset:52560
	ds_read_b128 v[50:53], v32 offset:52816
	s_waitcnt lgkmcnt(2)
	v_add_f32_e32 v7, v12, v16
	v_add_f32_e32 v12, v13, v17
	v_add_f32_e32 v13, v14, v18
	v_add_f32_e32 v14, v15, v19
	v_max_f32_e32 v68, 0, v7
	v_max_f32_e32 v70, 0, v12
	v_max_f32_e32 v72, 0, v13
	v_max_f32_e32 v86, 0, v14
	ds_read_b128 v[12:15], v32 offset:52368
	ds_read_b128 v[16:19], v32 offset:52624
	ds_read_b128 v[54:57], v32 offset:52880
	v_pk_fma_f32 v[88:89], v[4:5], v[24:25], 0 op_sel_hi:[1,0,0]
	v_mov_b32_e32 v28, v25
	v_mov_b32_e32 v24, v26
	v_mov_b32_e32 v25, v30
	v_mov_b32_e32 v30, v27
	s_waitcnt lgkmcnt(4)
	v_mov_b32_e32 v26, v20
	s_waitcnt lgkmcnt(3)
	v_mov_b32_e32 v27, v50
	v_mov_b32_e32 v50, v21
	v_mov_b32_e32 v20, v22
	v_mov_b32_e32 v21, v52
	v_mov_b32_e32 v52, v23
	v_pk_fma_f32 v[22:23], v[28:29], v[62:63], v[88:89] op_sel_hi:[1,0,1]
	v_mov_b32_e32 v4, v33
	v_pk_fma_f32 v[22:23], v[24:25], v[64:65], v[22:23] op_sel_hi:[1,0,1]
	v_mov_b32_e32 v5, v33
	v_pk_fma_f32 v[22:23], v[30:31], v[66:67], v[22:23] op_sel_hi:[1,0,1]
	s_waitcnt lgkmcnt(2)
	v_add_f32_e32 v7, v8, v12
	v_pk_fma_f32 v[22:23], v[26:27], v[68:69], v[22:23] op_sel_hi:[1,0,1]
	s_waitcnt lgkmcnt(1)
	v_mov_b32_e32 v8, v16
	v_pk_fma_f32 v[22:23], v[50:51], v[70:71], v[22:23] op_sel_hi:[1,0,1]
	v_add_f32_e32 v11, v11, v15
	v_pk_fma_f32 v[20:21], v[20:21], v[72:73], v[22:23] op_sel_hi:[1,0,1]
	v_add_f32_e32 v22, v9, v13
	v_pk_fma_f32 v[20:21], v[52:53], v[86:87], v[20:21] op_sel_hi:[1,0,1]
	v_add_f32_e32 v23, v10, v14
	s_waitcnt lgkmcnt(0)
	v_mov_b32_e32 v9, v54
	v_max_f32_e32 v10, 0, v7
	v_mov_b32_e32 v54, v17
	v_max_f32_e32 v14, 0, v22
	v_pk_fma_f32 v[8:9], v[8:9], v[10:11], v[20:21] op_sel_hi:[1,0,1]
	v_mov_b32_e32 v12, v18
	v_mov_b32_e32 v13, v56
	v_max_f32_e32 v16, 0, v23
	v_pk_fma_f32 v[8:9], v[54:55], v[14:15], v[8:9] op_sel_hi:[1,0,1]
	v_max_f32_e32 v22, 0, v11
	v_pk_fma_f32 v[8:9], v[12:13], v[16:17], v[8:9] op_sel_hi:[1,0,1]
	v_mov_b32_e32 v56, v19
	ds_read_b128 v[10:13], v32 offset:52432
	ds_read_b128 v[14:17], v32 offset:52688
	ds_read_b128 v[18:21], v32 offset:52944
	v_pk_fma_f32 v[22:23], v[56:57], v[22:23], v[8:9] op_sel_hi:[1,0,1]
	v_and_b32_e32 v24, 64, v84
	v_xor_b32_e32 v7, 16, v84
	v_add_u32_e32 v8, 64, v24
	v_cmp_lt_i32_e64 s[6:7], v7, v8
	s_and_b64 s[8:9], s[2:3], vcc
	s_waitcnt lgkmcnt(2)
	v_add_f32_e32 v9, v0, v10
	v_add_f32_e32 v11, v1, v11
	s_waitcnt lgkmcnt(1)
	v_mov_b32_e32 v0, v14
	s_waitcnt lgkmcnt(0)
	v_mov_b32_e32 v1, v18
	v_max_f32_e32 v10, 0, v9
	v_add_f32_e32 v24, v2, v12
	v_add_f32_e32 v13, v3, v13
	v_mov_b32_e32 v18, v15
	v_max_f32_e32 v12, 0, v11
	v_pk_fma_f32 v[0:1], v[0:1], v[10:11], v[22:23] op_sel_hi:[1,0,1]
	v_mov_b32_e32 v2, v16
	v_mov_b32_e32 v3, v20
	v_max_f32_e32 v14, 0, v24
	v_pk_fma_f32 v[0:1], v[18:19], v[12:13], v[0:1] op_sel_hi:[1,0,1]
	v_cndmask_b32_e64 v7, v84, v7, s[6:7]
	v_mov_b32_e32 v20, v17
	v_max_f32_e32 v16, 0, v13
	v_pk_fma_f32 v[0:1], v[2:3], v[14:15], v[0:1] op_sel_hi:[1,0,1]
	v_lshlrev_b32_e32 v7, 2, v7
	v_pk_fma_f32 v[0:1], v[20:21], v[16:17], v[0:1] op_sel_hi:[1,0,1]
	ds_bpermute_b32 v2, v7, v0
	ds_bpermute_b32 v3, v7, v1
	v_xor_b32_e32 v7, 32, v84
	v_cmp_lt_i32_e64 s[6:7], v7, v8
	v_mov_b32_e32 v10, -1
	s_waitcnt lgkmcnt(0)
	v_pk_add_f32 v[0:1], v[0:1], v[2:3]
	v_cndmask_b32_e64 v7, v84, v7, s[6:7]
	v_lshlrev_b32_e32 v7, 2, v7
	ds_bpermute_b32 v2, v7, v0
	ds_bpermute_b32 v3, v7, v1
	v_mov_b32_e32 v7, 0
	s_and_saveexec_b64 s[6:7], s[8:9]
	s_cbranch_execz .LBB5_108
	v_mov_b32_e32 v10, v103
	s_waitcnt lgkmcnt(0)
	v_pk_add_f32 v[4:5], v[0:1], v[2:3]
	v_mov_b32_e32 v7, 1.0

	.amdhsa_kernel _Z7k_layerILi2EEvPKDF16_PKiPKjS3_S3_S1_PKfPDF16_PhS3_S7_Pf
		.amdhsa_group_segment_fixed_size 35584
		.amdhsa_private_segment_fixed_size 0
		.amdhsa_kernarg_size 352
		.amdhsa_user_sgpr_count 2
		.amdhsa_user_sgpr_dispatch_ptr 0
		.amdhsa_user_sgpr_queue_ptr 0
		.amdhsa_user_sgpr_kernarg_segment_ptr 1
		.amdhsa_user_sgpr_dispatch_id 0
		.amdhsa_user_sgpr_kernarg_preload_length 0
		.amdhsa_user_sgpr_kernarg_preload_offset 0
		.amdhsa_user_sgpr_private_segment_size 0
		.amdhsa_uses_dynamic_stack 0
		.amdhsa_enable_private_segment 0
		.amdhsa_system_sgpr_workgroup_id_x 1
		.amdhsa_system_sgpr_workgroup_id_y 0
		.amdhsa_system_sgpr_workgroup_id_z 0
		.amdhsa_system_sgpr_workgroup_info 0
		.amdhsa_system_vgpr_workitem_id 0
		.amdhsa_next_free_vgpr 104
		.amdhsa_next_free_sgpr 42
		.amdhsa_accum_offset 104
		.amdhsa_reserve_vcc 1
		.amdhsa_float_round_mode_32 0
		.amdhsa_float_round_mode_16_64 0
		.amdhsa_float_denorm_mode_32 3
		.amdhsa_float_denorm_mode_16_64 3
		.amdhsa_dx10_clamp 1
		.amdhsa_ieee_mode 1
		.amdhsa_fp16_overflow 0
		.amdhsa_tg_split 0
		.amdhsa_exception_fp_ieee_invalid_op 0
		.amdhsa_exception_fp_denorm_src 0
		.amdhsa_exception_fp_ieee_div_zero 0
		.amdhsa_exception_fp_ieee_overflow 0
		.amdhsa_exception_fp_ieee_underflow 0
		.amdhsa_exception_fp_ieee_inexact 0
		.amdhsa_exception_int_div_zero 0
	.end_amdhsa_kernel

amdhsa.kernels:
  - .agpr_count:     0
    .args:
      - .actual_access:  read_only
        .address_space:  global
        .offset:         0
        .size:           8
        .value_kind:     global_buffer
      - .actual_access:  read_only
        .address_space:  global
        .offset:         8
        .size:           8
        .value_kind:     global_buffer
      - .actual_access:  read_only
        .address_space:  global
        .offset:         16
        .size:           8
        .value_kind:     global_buffer
      - .actual_access:  read_only
        .address_space:  global
        .offset:         24
        .size:           8
        .value_kind:     global_buffer
      - .actual_access:  read_only
        .address_space:  global
        .offset:         32
        .size:           8
        .value_kind:     global_buffer
      - .actual_access:  read_only
        .address_space:  global
        .offset:         40
        .size:           8
        .value_kind:     global_buffer
      - .actual_access:  read_only
        .address_space:  global
        .offset:         48
        .size:           8
        .value_kind:     global_buffer
      - .actual_access:  read_only
        .address_space:  global
        .offset:         56
        .size:           8
        .value_kind:     global_buffer
      - .actual_access:  read_only
        .address_space:  global
        .offset:         64
        .size:           8
        .value_kind:     global_buffer
      - .actual_access:  read_only
        .address_space:  global
        .offset:         72
        .size:           8
        .value_kind:     global_buffer
      - .actual_access:  read_only
        .address_space:  global
        .offset:         80
        .size:           8
        .value_kind:     global_buffer
      - .actual_access:  read_only
        .address_space:  global
        .offset:         88
        .size:           8
        .value_kind:     global_buffer
      - .actual_access:  write_only
        .address_space:  global
        .offset:         96
        .size:           8
        .value_kind:     global_buffer
      - .actual_access:  write_only
        .address_space:  global
        .offset:         104
        .size:           8
        .value_kind:     global_buffer
      - .actual_access:  write_only
        .address_space:  global
        .offset:         112
        .size:           8
        .value_kind:     global_buffer
      - .actual_access:  write_only
        .address_space:  global
        .offset:         120
        .size:           8
        .value_kind:     global_buffer
      - .actual_access:  write_only
        .address_space:  global
        .offset:         128
        .size:           8
        .value_kind:     global_buffer
      - .actual_access:  write_only
        .address_space:  global
        .offset:         136
        .size:           8
        .value_kind:     global_buffer
      - .actual_access:  write_only
        .address_space:  global
        .offset:         144
        .size:           8
        .value_kind:     global_buffer
      - .actual_access:  write_only
        .address_space:  global
        .offset:         152
        .size:           8
        .value_kind:     global_buffer
      - .actual_access:  write_only
        .address_space:  global
        .offset:         160
        .size:           8
        .value_kind:     global_buffer
    .group_segment_fixed_size: 0
    .kernarg_segment_align: 8
    .kernarg_segment_size: 168
    .language:       OpenCL C
    .language_version:
      - 2
      - 0
    .max_flat_workgroup_size: 1024
    .name:           _Z6k_prepPKiS0_PKfS2_S2_S2_S2_S2_S2_S2_S2_S2_PDF16_S3_S3_PfS4_S4_PjS3_S5_
    .private_segment_fixed_size: 0
    .sgpr_count:     27
    .sgpr_spill_count: 0
    .symbol:         _Z6k_prepPKiS0_PKfS2_S2_S2_S2_S2_S2_S2_S2_S2_PDF16_S3_S3_PfS4_S4_PjS3_S5_.kd
    .uniform_work_group_size: 1
    .uses_dynamic_stack: false
    .vgpr_count:     61
    .vgpr_spill_count: 0
    .wavefront_size: 64
  - .agpr_count:     0
    .args:
      - .actual_access:  read_only
        .address_space:  global
        .offset:         0
        .size:           8
        .value_kind:     global_buffer
      - .actual_access:  read_only
        .address_space:  global
        .offset:         8
        .size:           8
        .value_kind:     global_buffer
      - .actual_access:  read_only
        .address_space:  global
        .offset:         16
        .size:           8
        .value_kind:     global_buffer
      - .actual_access:  write_only
        .address_space:  global
        .offset:         24
        .size:           8
        .value_kind:     global_buffer
      - .actual_access:  write_only
        .address_space:  global
        .offset:         32
        .size:           8
        .value_kind:     global_buffer
      - .actual_access:  write_only
        .address_space:  global
        .offset:         40
        .size:           8
        .value_kind:     global_buffer
      - .actual_access:  read_only
        .address_space:  global
        .offset:         48
        .size:           8
        .value_kind:     global_buffer
      - .actual_access:  read_only
        .address_space:  global
        .offset:         56
        .size:           8
        .value_kind:     global_buffer
      - .actual_access:  read_only
        .address_space:  global
        .offset:         64
        .size:           8
        .value_kind:     global_buffer
      - .actual_access:  read_only
        .address_space:  global
        .offset:         72
        .size:           8
        .value_kind:     global_buffer
      - .actual_access:  read_only
        .address_space:  global
        .offset:         80
        .size:           8
        .value_kind:     global_buffer
      - .actual_access:  read_only
        .address_space:  global
        .offset:         88
        .size:           8
        .value_kind:     global_buffer
      - .actual_access:  read_only
        .address_space:  global
        .offset:         96
        .size:           8
        .value_kind:     global_buffer
      - .actual_access:  read_only
        .address_space:  global
        .offset:         104
        .size:           8
        .value_kind:     global_buffer
      - .actual_access:  read_only
        .address_space:  global
        .offset:         112
        .size:           8
        .value_kind:     global_buffer
      - .actual_access:  read_only
        .address_space:  global
        .offset:         120
        .size:           8
        .value_kind:     global_buffer
      - .actual_access:  read_only
        .address_space:  global
        .offset:         128
        .size:           8
        .value_kind:     global_buffer
      - .actual_access:  write_only
        .address_space:  global
        .offset:         136
        .size:           8
        .value_kind:     global_buffer
      - .actual_access:  write_only
        .address_space:  global
        .offset:         144
        .size:           8
        .value_kind:     global_buffer
      - .actual_access:  write_only
        .address_space:  global
        .offset:         152
        .size:           8
        .value_kind:     global_buffer
      - .actual_access:  write_only
        .address_space:  global
        .offset:         160
        .size:           8
        .value_kind:     global_buffer
      - .actual_access:  write_only
        .address_space:  global
        .offset:         168
        .size:           8
        .value_kind:     global_buffer
    .group_segment_fixed_size: 1696
    .kernarg_segment_align: 8
    .kernarg_segment_size: 176
    .language:       OpenCL C
    .language_version:
      - 2
      - 0
    .max_flat_workgroup_size: 1024
    .name:           _Z11k_localsortPKiS0_S0_PjPtPiPKjPKfS7_S7_S7_S7_S7_S7_S7_S7_S7_PDF16_S8_S8_PfS9_
    .private_segment_fixed_size: 0
    .sgpr_count:     71
    .sgpr_spill_count: 0
    .symbol:         _Z11k_localsortPKiS0_S0_PjPtPiPKjPKfS7_S7_S7_S7_S7_S7_S7_S7_S7_PDF16_S8_S8_PfS9_.kd
    .uniform_work_group_size: 1
    .uses_dynamic_stack: false
    .vgpr_count:     95
    .vgpr_spill_count: 0
    .wavefront_size: 64
  - .agpr_count:     0
    .args:
      - .actual_access:  read_only
        .address_space:  global
        .offset:         0
        .size:           8
        .value_kind:     global_buffer
      - .actual_access:  read_only
        .address_space:  global
        .offset:         8
        .size:           8
        .value_kind:     global_buffer
      - .actual_access:  read_only
        .address_space:  global
        .offset:         16
        .size:           8
        .value_kind:     global_buffer
      - .actual_access:  write_only
        .address_space:  global
        .offset:         24
        .size:           8
        .value_kind:     global_buffer
      - .actual_access:  write_only
        .address_space:  global
        .offset:         32
        .size:           8
        .value_kind:     global_buffer
    .group_segment_fixed_size: 54144
    .kernarg_segment_align: 8
    .kernarg_segment_size: 40
    .language:       OpenCL C
    .language_version:
      - 2
      - 0
    .max_flat_workgroup_size: 1024
    .name:           _Z12k_bucketsortPKjPKtPKiPiPj
    .private_segment_fixed_size: 0
    .sgpr_count:     70
    .sgpr_spill_count: 0
    .symbol:         _Z12k_bucketsortPKjPKtPKiPiPj.kd
    .uniform_work_group_size: 1
    .uses_dynamic_stack: false
    .vgpr_count:     59
    .vgpr_spill_count: 0
    .wavefront_size: 64
  - .agpr_count:     0
    .args:
      - .actual_access:  read_only
        .address_space:  global
        .offset:         0
        .size:           8
        .value_kind:     global_buffer
      - .actual_access:  read_only
        .address_space:  global
        .offset:         8
        .size:           8
        .value_kind:     global_buffer
      - .actual_access:  write_only
        .address_space:  global
        .offset:         16
        .size:           8
        .value_kind:     global_buffer
    .group_segment_fixed_size: 0
    .kernarg_segment_align: 8
    .kernarg_segment_size: 24
    .language:       OpenCL C
    .language_version:
      - 2
      - 0
    .max_flat_workgroup_size: 256
    .name:           _Z7k_finalPKfS0_Pf
    .private_segment_fixed_size: 0
    .sgpr_count:     14
    .sgpr_spill_count: 0
    .symbol:         _Z7k_finalPKfS0_Pf.kd
    .uniform_work_group_size: 1
    .uses_dynamic_stack: false
    .vgpr_count:     10
    .vgpr_spill_count: 0
    .wavefront_size: 64
  - .agpr_count:     0
    .args:
      - .actual_access:  read_only
        .address_space:  global
        .offset:         0
        .size:           8
        .value_kind:     global_buffer
      - .actual_access:  read_only
        .address_space:  global
        .offset:         8
        .size:           8
        .value_kind:     global_buffer
      - .actual_access:  read_only
        .address_space:  global
        .offset:         16
        .size:           8
        .value_kind:     global_buffer
      - .actual_access:  read_only
        .address_space:  global
        .offset:         24
        .size:           8
        .value_kind:     global_buffer
      - .actual_access:  read_only
        .address_space:  global
        .offset:         32
        .size:           8
        .value_kind:     global_buffer
      - .actual_access:  read_only
        .address_space:  global
        .offset:         40
        .size:           8
        .value_kind:     global_buffer
      - .address_space:  global
        .offset:         48
        .size:           8
        .value_kind:     global_buffer
      - .actual_access:  write_only
        .address_space:  global
        .offset:         56
        .size:           8
        .value_kind:     global_buffer
      - .address_space:  global
        .offset:         64
        .size:           8
        .value_kind:     global_buffer
      - .actual_access:  read_only
        .address_space:  global
        .offset:         72
        .size:           8
        .value_kind:     global_buffer
      - .address_space:  global
        .offset:         80
        .size:           8
        .value_kind:     global_buffer
      - .actual_access:  read_only
        .address_space:  global
        .offset:         88
        .size:           8
        .value_kind:     global_buffer
      - .offset:         96
        .size:           4
        .value_kind:     hidden_block_count_x
      - .offset:         100
        .size:           4
        .value_kind:     hidden_block_count_y
      - .offset:         104
        .size:           4
        .value_kind:     hidden_block_count_z
      - .offset:         108
        .size:           2
        .value_kind:     hidden_group_size_x
      - .offset:         110
        .size:           2
        .value_kind:     hidden_group_size_y
      - .offset:         112
        .size:           2
        .value_kind:     hidden_group_size_z
      - .offset:         114
        .size:           2
        .value_kind:     hidden_remainder_x
      - .offset:         116
        .size:           2
        .value_kind:     hidden_remainder_y
      - .offset:         118
        .size:           2
        .value_kind:     hidden_remainder_z
      - .offset:         136
        .size:           8
        .value_kind:     hidden_global_offset_x
      - .offset:         144
        .size:           8
        .value_kind:     hidden_global_offset_y
      - .offset:         152
        .size:           8
        .value_kind:     hidden_global_offset_z
      - .offset:         160
        .size:           2
        .value_kind:     hidden_grid_dims
      - .offset:         216
        .size:           4
        .value_kind:     hidden_dynamic_lds_size
    .group_segment_fixed_size: 35072
    .kernarg_segment_align: 8
    .kernarg_segment_size: 352
    .language:       OpenCL C
    .language_version:
      - 2
      - 0
    .max_flat_workgroup_size: 1024
    .name:           _Z7k_layerILi1EEvPKDF16_PKiPKjS3_S3_S1_PKfPDF16_PhS3_S7_Pf
    .private_segment_fixed_size: 0
    .sgpr_count:     43
    .sgpr_spill_count: 0
    .symbol:         _Z7k_layerILi1EEvPKDF16_PKiPKjS3_S3_S1_PKfPDF16_PhS3_S7_Pf.kd
    .uniform_work_group_size: 1
    .uses_dynamic_stack: false
    .vgpr_count:     116
    .vgpr_spill_count: 0
    .wavefront_size: 64
  - .agpr_count:     0
    .args:
      - .actual_access:  read_only
        .address_space:  global
        .offset:         0
        .size:           8
        .value_kind:     global_buffer
      - .actual_access:  read_only
        .address_space:  global
        .offset:         8
        .size:           8
        .value_kind:     global_buffer
      - .actual_access:  read_only
        .address_space:  global
        .offset:         16
        .size:           8
        .value_kind:     global_buffer
      - .actual_access:  read_only
        .address_space:  global
        .offset:         24
        .size:           8
        .value_kind:     global_buffer
      - .actual_access:  read_only
        .address_space:  global
        .offset:         32
        .size:           8
        .value_kind:     global_buffer
      - .actual_access:  read_only
        .address_space:  global
        .offset:         40
        .size:           8
        .value_kind:     global_buffer
      - .address_space:  global
        .offset:         48
        .size:           8
        .value_kind:     global_buffer
      - .actual_access:  read_only
        .address_space:  global
        .offset:         56
        .size:           8
        .value_kind:     global_buffer
      - .address_space:  global
        .offset:         64
        .size:           8
        .value_kind:     global_buffer
      - .actual_access:  read_only
        .address_space:  global
        .offset:         72
        .size:           8
        .value_kind:     global_buffer
      - .address_space:  global
        .offset:         80
        .size:           8
        .value_kind:     global_buffer
      - .address_space:  global
        .offset:         88
        .size:           8
        .value_kind:     global_buffer
      - .offset:         96
        .size:           4
        .value_kind:     hidden_block_count_x
      - .offset:         100
        .size:           4
        .value_kind:     hidden_block_count_y
      - .offset:         104
        .size:           4
        .value_kind:     hidden_block_count_z
      - .offset:         108
        .size:           2
        .value_kind:     hidden_group_size_x
      - .offset:         110
        .size:           2
        .value_kind:     hidden_group_size_y
      - .offset:         112
        .size:           2
        .value_kind:     hidden_group_size_z
      - .offset:         114
        .size:           2
        .value_kind:     hidden_remainder_x
      - .offset:         116
        .size:           2
        .value_kind:     hidden_remainder_y
      - .offset:         118
        .size:           2
        .value_kind:     hidden_remainder_z
      - .offset:         136
        .size:           8
        .value_kind:     hidden_global_offset_x
      - .offset:         144
        .size:           8
        .value_kind:     hidden_global_offset_y
      - .offset:         152
        .size:           8
        .value_kind:     hidden_global_offset_z
      - .offset:         160
        .size:           2
        .value_kind:     hidden_grid_dims
      - .offset:         216
        .size:           4
        .value_kind:     hidden_dynamic_lds_size
    .group_segment_fixed_size: 35584
    .kernarg_segment_align: 8
    .kernarg_segment_size: 352
    .language:       OpenCL C
    .language_version:
      - 2
      - 0
    .max_flat_workgroup_size: 1024
    .name:           _Z7k_layerILi2EEvPKDF16_PKiPKjS3_S3_S1_PKfPDF16_PhS3_S7_Pf
    .private_segment_fixed_size: 0
    .sgpr_count:     48
    .sgpr_spill_count: 0
    .symbol:         _Z7k_layerILi2EEvPKDF16_PKiPKjS3_S3_S1_PKfPDF16_PhS3_S7_Pf.kd
    .uniform_work_group_size: 1
    .uses_dynamic_stack: false
    .vgpr_count:     104
    .vgpr_spill_count: 0
    .wavefront_size: 64
